# diff-attention epilogue hand-written: 16 row reductions batched through DPP/permlane16 (no bpermute chain), rows staged in the wave's dead Q tile and stored as 8 dwordx4 instead of 64 short stores
# speedup vs baseline: 1.0060x; 1.0060x over previous
.LBB0_563:
	v_mov_b32_e32 v230, 0xff800000
	v_mov_b32_e32 v228, v251
	v_mov_b32_e32 v229, v208
	s_nop 1
	v_permlane32_swap_b32_e32 v251, v228
	v_permlane32_swap_b32_e32 v208, v229
	v_add_f32_e32 v251, v251, v228
	v_add_f32_e32 v208, v208, v229
	s_or_b32 s14, s39, s35
	s_mul_hi_i32 s18, s14, 0x1a00
	s_mul_i32 s16, s14, 0x1a00
	v_div_scale_f32 v129, s[14:15], v251, v251, 1.0
	v_rcp_f32_e32 v130, v129
	s_add_u32 s14, s36, s16
	v_div_scale_f32 v147, s[16:17], v208, v208, v232
	v_fma_f32 v131, -v129, v130, 1.0
	v_fmac_f32_e32 v130, v131, v130
	v_div_scale_f32 v131, vcc, 1.0, v251, 1.0
	v_rcp_f32_e32 v148, v147
	v_mul_f32_e32 v132, v131, v130
	v_fma_f32 v133, -v129, v132, v131
	v_fmac_f32_e32 v132, v133, v130
	v_fma_f32 v129, -v129, v132, v131
	v_fma_f32 v149, -v147, v148, 1.0
	v_div_fmas_f32 v129, v129, v130, v132
	v_fmac_f32_e32 v148, v149, v148
	v_div_scale_f32 v149, vcc, v232, v208, v232
	v_mul_f32_e32 v150, v149, v148
	v_fma_f32 v151, -v147, v150, v149
	v_fmac_f32_e32 v150, v151, v148
	v_fma_f32 v147, -v147, v150, v149
	v_div_fixup_f32 v129, v129, v251, 1.0
	v_ashrrev_i32_e32 v128, 5, v235
	v_lshl_add_u32 v146, v235, 2, s40
	v_div_fmas_f32 v147, v147, v148, v150
	ds_write_b32 v146, v129
	v_lshl_add_u32 v129, v128, 4, s40
	v_div_fixup_f32 v147, v147, v208, v232
	ds_read_b128 v[130:133], v129
	ds_read_b128 v[134:137], v129 offset:32
	ds_read_b128 v[138:141], v129 offset:64
	ds_read_b128 v[142:145], v129 offset:96
	ds_write_b32 v146, v147
	ds_read_b128 v[146:149], v129
	ds_read_b128 v[150:153], v129 offset:32
	ds_read_b128 v[154:157], v129 offset:64
	ds_read_b128 v[158:161], v129 offset:96
	s_addc_u32 s15, s37, s18
	s_waitcnt lgkmcnt(0)
	v_and_b32_e32 v199, 31, v235
	v_lshlrev_b32_e32 v198, 2, v199
	global_load_dword v194, v198, s[4:5]
	global_load_dword v195, v198, s[4:5] offset:128
	global_load_dword v196, v198, s[4:5] offset:256
	global_load_dword v197, v198, s[4:5] offset:384
	v_mul_f32_e32 v112, v112, v146
	v_mul_f32_e32 v113, v113, v147
	v_mul_f32_e32 v114, v114, v148
	v_mul_f32_e32 v115, v115, v149
	v_mul_f32_e32 v116, v116, v150
	v_mul_f32_e32 v117, v117, v151
	v_mul_f32_e32 v118, v118, v152
	v_mul_f32_e32 v119, v119, v153
	v_mul_f32_e32 v120, v120, v154
	v_mul_f32_e32 v121, v121, v155
	v_mul_f32_e32 v122, v122, v156
	v_mul_f32_e32 v123, v123, v157
	v_mul_f32_e32 v124, v124, v158
	v_mul_f32_e32 v125, v125, v159
	v_mul_f32_e32 v126, v126, v160
	v_mul_f32_e32 v127, v127, v161
	v_fma_f32 v64, v64, v130, -v112
	v_fma_f32 v65, v65, v131, -v113
	v_fma_f32 v66, v66, v132, -v114
	v_fma_f32 v67, v67, v133, -v115
	v_fma_f32 v68, v68, v134, -v116
	v_fma_f32 v69, v69, v135, -v117
	v_fma_f32 v70, v70, v136, -v118
	v_fma_f32 v71, v71, v137, -v119
	v_fma_f32 v72, v72, v138, -v120
	v_fma_f32 v73, v73, v139, -v121
	v_fma_f32 v74, v74, v140, -v122
	v_fma_f32 v75, v75, v141, -v123
	v_fma_f32 v76, v76, v142, -v124
	v_fma_f32 v77, v77, v143, -v125
	v_fma_f32 v78, v78, v144, -v126
	v_fma_f32 v79, v79, v145, -v127
	v_mul_f32_e32 v96, v96, v146
	v_mul_f32_e32 v97, v97, v147
	v_mul_f32_e32 v98, v98, v148
	v_mul_f32_e32 v99, v99, v149
	v_mul_f32_e32 v100, v100, v150
	v_mul_f32_e32 v101, v101, v151
	v_mul_f32_e32 v102, v102, v152
	v_mul_f32_e32 v103, v103, v153
	v_mul_f32_e32 v104, v104, v154
	v_mul_f32_e32 v105, v105, v155
	v_mul_f32_e32 v106, v106, v156
	v_mul_f32_e32 v107, v107, v157
	v_mul_f32_e32 v108, v108, v158
	v_mul_f32_e32 v109, v109, v159
	v_mul_f32_e32 v110, v110, v160
	v_mul_f32_e32 v111, v111, v161
	v_fma_f32 v32, v32, v130, -v96
	v_fma_f32 v33, v33, v131, -v97
	v_fma_f32 v34, v34, v132, -v98
	v_fma_f32 v35, v35, v133, -v99
	v_fma_f32 v36, v36, v134, -v100
	v_fma_f32 v37, v37, v135, -v101
	v_fma_f32 v38, v38, v136, -v102
	v_fma_f32 v39, v39, v137, -v103
	v_fma_f32 v40, v40, v138, -v104
	v_fma_f32 v41, v41, v139, -v105
	v_fma_f32 v42, v42, v140, -v106
	v_fma_f32 v43, v43, v141, -v107
	v_fma_f32 v44, v44, v142, -v108
	v_fma_f32 v45, v45, v143, -v109
	v_fma_f32 v46, v46, v144, -v110
	v_fma_f32 v47, v47, v145, -v111
	v_mul_f32_e32 v80, v80, v146
	v_mul_f32_e32 v81, v81, v147
	v_mul_f32_e32 v82, v82, v148
	v_mul_f32_e32 v83, v83, v149
	v_mul_f32_e32 v84, v84, v150
	v_mul_f32_e32 v85, v85, v151
	v_mul_f32_e32 v86, v86, v152
	v_mul_f32_e32 v87, v87, v153
	v_mul_f32_e32 v88, v88, v154
	v_mul_f32_e32 v89, v89, v155
	v_mul_f32_e32 v90, v90, v156
	v_mul_f32_e32 v91, v91, v157
	v_mul_f32_e32 v92, v92, v158
	v_mul_f32_e32 v93, v93, v159
	v_mul_f32_e32 v94, v94, v160
	v_mul_f32_e32 v95, v95, v161
	v_fma_f32 v16, v16, v130, -v80
	v_fma_f32 v17, v17, v131, -v81
	v_fma_f32 v18, v18, v132, -v82
	v_fma_f32 v19, v19, v133, -v83
	v_fma_f32 v20, v20, v134, -v84
	v_fma_f32 v21, v21, v135, -v85
	v_fma_f32 v22, v22, v136, -v86
	v_fma_f32 v23, v23, v137, -v87
	v_fma_f32 v24, v24, v138, -v88
	v_fma_f32 v25, v25, v139, -v89
	v_fma_f32 v26, v26, v140, -v90
	v_fma_f32 v27, v27, v141, -v91
	v_fma_f32 v28, v28, v142, -v92
	v_fma_f32 v29, v29, v143, -v93
	v_fma_f32 v30, v30, v144, -v94
	v_fma_f32 v31, v31, v145, -v95
	v_mul_f32_e32 v48, v48, v146
	v_mul_f32_e32 v49, v49, v147
	v_mul_f32_e32 v50, v50, v148
	v_mul_f32_e32 v51, v51, v149
	v_mul_f32_e32 v52, v52, v150
	v_mul_f32_e32 v53, v53, v151
	v_mul_f32_e32 v54, v54, v152
	v_mul_f32_e32 v55, v55, v153
	v_mul_f32_e32 v56, v56, v154
	v_mul_f32_e32 v57, v57, v155
	v_mul_f32_e32 v58, v58, v156
	v_mul_f32_e32 v59, v59, v157
	v_mul_f32_e32 v60, v60, v158
	v_mul_f32_e32 v61, v61, v159
	v_mul_f32_e32 v62, v62, v160
	v_mul_f32_e32 v63, v63, v161
	v_fma_f32 v0, v0, v130, -v48
	v_fma_f32 v1, v1, v131, -v49
	v_fma_f32 v2, v2, v132, -v50
	v_fma_f32 v3, v3, v133, -v51
	v_fma_f32 v4, v4, v134, -v52
	v_fma_f32 v5, v5, v135, -v53
	v_fma_f32 v6, v6, v136, -v54
	v_fma_f32 v7, v7, v137, -v55
	v_fma_f32 v8, v8, v138, -v56
	v_fma_f32 v9, v9, v139, -v57
	v_fma_f32 v10, v10, v140, -v58
	v_fma_f32 v11, v11, v141, -v59
	v_fma_f32 v12, v12, v142, -v60
	v_fma_f32 v13, v13, v143, -v61
	v_fma_f32 v14, v14, v144, -v62
	v_fma_f32 v15, v15, v145, -v63
	v_mul_f32_e32 v162, v32, v32
	v_mul_f32_e32 v163, v33, v33
	v_mul_f32_e32 v164, v34, v34
	v_mul_f32_e32 v165, v35, v35
	v_mul_f32_e32 v166, v36, v36
	v_mul_f32_e32 v167, v37, v37
	v_mul_f32_e32 v168, v38, v38
	v_mul_f32_e32 v169, v39, v39
	v_mul_f32_e32 v170, v40, v40
	v_mul_f32_e32 v171, v41, v41
	v_mul_f32_e32 v172, v42, v42
	v_mul_f32_e32 v173, v43, v43
	v_mul_f32_e32 v174, v44, v44
	v_mul_f32_e32 v175, v45, v45
	v_mul_f32_e32 v176, v46, v46
	v_mul_f32_e32 v177, v47, v47
	v_fmac_f32_e32 v162, v64, v64
	v_fmac_f32_e32 v163, v65, v65
	v_fmac_f32_e32 v164, v66, v66
	v_fmac_f32_e32 v165, v67, v67
	v_fmac_f32_e32 v166, v68, v68
	v_fmac_f32_e32 v167, v69, v69
	v_fmac_f32_e32 v168, v70, v70
	v_fmac_f32_e32 v169, v71, v71
	v_fmac_f32_e32 v170, v72, v72
	v_fmac_f32_e32 v171, v73, v73
	v_fmac_f32_e32 v172, v74, v74
	v_fmac_f32_e32 v173, v75, v75
	v_fmac_f32_e32 v174, v76, v76
	v_fmac_f32_e32 v175, v77, v77
	v_fmac_f32_e32 v176, v78, v78
	v_fmac_f32_e32 v177, v79, v79
	v_fmac_f32_e32 v162, v16, v16
	v_fmac_f32_e32 v163, v17, v17
	v_fmac_f32_e32 v164, v18, v18
	v_fmac_f32_e32 v165, v19, v19
	v_fmac_f32_e32 v166, v20, v20
	v_fmac_f32_e32 v167, v21, v21
	v_fmac_f32_e32 v168, v22, v22
	v_fmac_f32_e32 v169, v23, v23
	v_fmac_f32_e32 v170, v24, v24
	v_fmac_f32_e32 v171, v25, v25
	v_fmac_f32_e32 v172, v26, v26
	v_fmac_f32_e32 v173, v27, v27
	v_fmac_f32_e32 v174, v28, v28
	v_fmac_f32_e32 v175, v29, v29
	v_fmac_f32_e32 v176, v30, v30
	v_fmac_f32_e32 v177, v31, v31
	v_fmac_f32_e32 v162, v0, v0
	v_fmac_f32_e32 v163, v1, v1
	v_fmac_f32_e32 v164, v2, v2
	v_fmac_f32_e32 v165, v3, v3
	v_fmac_f32_e32 v166, v4, v4
	v_fmac_f32_e32 v167, v5, v5
	v_fmac_f32_e32 v168, v6, v6
	v_fmac_f32_e32 v169, v7, v7
	v_fmac_f32_e32 v170, v8, v8
	v_fmac_f32_e32 v171, v9, v9
	v_fmac_f32_e32 v172, v10, v10
	v_fmac_f32_e32 v173, v11, v11
	v_fmac_f32_e32 v174, v12, v12
	v_fmac_f32_e32 v175, v13, v13
	v_fmac_f32_e32 v176, v14, v14
	v_fmac_f32_e32 v177, v15, v15
	v_add_f32_dpp v162, v162, v162 quad_perm:[1,0,3,2] row_mask:0xf bank_mask:0xf
	v_add_f32_dpp v163, v163, v163 quad_perm:[1,0,3,2] row_mask:0xf bank_mask:0xf
	v_add_f32_dpp v164, v164, v164 quad_perm:[1,0,3,2] row_mask:0xf bank_mask:0xf
	v_add_f32_dpp v165, v165, v165 quad_perm:[1,0,3,2] row_mask:0xf bank_mask:0xf
	v_add_f32_dpp v166, v166, v166 quad_perm:[1,0,3,2] row_mask:0xf bank_mask:0xf
	v_add_f32_dpp v167, v167, v167 quad_perm:[1,0,3,2] row_mask:0xf bank_mask:0xf
	v_add_f32_dpp v168, v168, v168 quad_perm:[1,0,3,2] row_mask:0xf bank_mask:0xf
	v_add_f32_dpp v169, v169, v169 quad_perm:[1,0,3,2] row_mask:0xf bank_mask:0xf
	v_add_f32_dpp v170, v170, v170 quad_perm:[1,0,3,2] row_mask:0xf bank_mask:0xf
	v_add_f32_dpp v171, v171, v171 quad_perm:[1,0,3,2] row_mask:0xf bank_mask:0xf
	v_add_f32_dpp v172, v172, v172 quad_perm:[1,0,3,2] row_mask:0xf bank_mask:0xf
	v_add_f32_dpp v173, v173, v173 quad_perm:[1,0,3,2] row_mask:0xf bank_mask:0xf
	v_add_f32_dpp v174, v174, v174 quad_perm:[1,0,3,2] row_mask:0xf bank_mask:0xf
	v_add_f32_dpp v175, v175, v175 quad_perm:[1,0,3,2] row_mask:0xf bank_mask:0xf
	v_add_f32_dpp v176, v176, v176 quad_perm:[1,0,3,2] row_mask:0xf bank_mask:0xf
	v_add_f32_dpp v177, v177, v177 quad_perm:[1,0,3,2] row_mask:0xf bank_mask:0xf
	v_add_f32_dpp v162, v162, v162 quad_perm:[2,3,0,1] row_mask:0xf bank_mask:0xf
	v_add_f32_dpp v163, v163, v163 quad_perm:[2,3,0,1] row_mask:0xf bank_mask:0xf
	v_add_f32_dpp v164, v164, v164 quad_perm:[2,3,0,1] row_mask:0xf bank_mask:0xf
	v_add_f32_dpp v165, v165, v165 quad_perm:[2,3,0,1] row_mask:0xf bank_mask:0xf
	v_add_f32_dpp v166, v166, v166 quad_perm:[2,3,0,1] row_mask:0xf bank_mask:0xf
	v_add_f32_dpp v167, v167, v167 quad_perm:[2,3,0,1] row_mask:0xf bank_mask:0xf
	v_add_f32_dpp v168, v168, v168 quad_perm:[2,3,0,1] row_mask:0xf bank_mask:0xf
	v_add_f32_dpp v169, v169, v169 quad_perm:[2,3,0,1] row_mask:0xf bank_mask:0xf
	v_add_f32_dpp v170, v170, v170 quad_perm:[2,3,0,1] row_mask:0xf bank_mask:0xf
	v_add_f32_dpp v171, v171, v171 quad_perm:[2,3,0,1] row_mask:0xf bank_mask:0xf
	v_add_f32_dpp v172, v172, v172 quad_perm:[2,3,0,1] row_mask:0xf bank_mask:0xf
	v_add_f32_dpp v173, v173, v173 quad_perm:[2,3,0,1] row_mask:0xf bank_mask:0xf
	v_add_f32_dpp v174, v174, v174 quad_perm:[2,3,0,1] row_mask:0xf bank_mask:0xf
	v_add_f32_dpp v175, v175, v175 quad_perm:[2,3,0,1] row_mask:0xf bank_mask:0xf
	v_add_f32_dpp v176, v176, v176 quad_perm:[2,3,0,1] row_mask:0xf bank_mask:0xf
	v_add_f32_dpp v177, v177, v177 quad_perm:[2,3,0,1] row_mask:0xf bank_mask:0xf
	v_add_f32_dpp v162, v162, v162 row_half_mirror row_mask:0xf bank_mask:0xf
	v_add_f32_dpp v163, v163, v163 row_half_mirror row_mask:0xf bank_mask:0xf
	v_add_f32_dpp v164, v164, v164 row_half_mirror row_mask:0xf bank_mask:0xf
	v_add_f32_dpp v165, v165, v165 row_half_mirror row_mask:0xf bank_mask:0xf
	v_add_f32_dpp v166, v166, v166 row_half_mirror row_mask:0xf bank_mask:0xf
	v_add_f32_dpp v167, v167, v167 row_half_mirror row_mask:0xf bank_mask:0xf
	v_add_f32_dpp v168, v168, v168 row_half_mirror row_mask:0xf bank_mask:0xf
	v_add_f32_dpp v169, v169, v169 row_half_mirror row_mask:0xf bank_mask:0xf
	v_add_f32_dpp v170, v170, v170 row_half_mirror row_mask:0xf bank_mask:0xf
	v_add_f32_dpp v171, v171, v171 row_half_mirror row_mask:0xf bank_mask:0xf
	v_add_f32_dpp v172, v172, v172 row_half_mirror row_mask:0xf bank_mask:0xf
	v_add_f32_dpp v173, v173, v173 row_half_mirror row_mask:0xf bank_mask:0xf
	v_add_f32_dpp v174, v174, v174 row_half_mirror row_mask:0xf bank_mask:0xf
	v_add_f32_dpp v175, v175, v175 row_half_mirror row_mask:0xf bank_mask:0xf
	v_add_f32_dpp v176, v176, v176 row_half_mirror row_mask:0xf bank_mask:0xf
	v_add_f32_dpp v177, v177, v177 row_half_mirror row_mask:0xf bank_mask:0xf
	v_add_f32_dpp v162, v162, v162 row_mirror row_mask:0xf bank_mask:0xf
	v_add_f32_dpp v163, v163, v163 row_mirror row_mask:0xf bank_mask:0xf
	v_add_f32_dpp v164, v164, v164 row_mirror row_mask:0xf bank_mask:0xf
	v_add_f32_dpp v165, v165, v165 row_mirror row_mask:0xf bank_mask:0xf
	v_add_f32_dpp v166, v166, v166 row_mirror row_mask:0xf bank_mask:0xf
	v_add_f32_dpp v167, v167, v167 row_mirror row_mask:0xf bank_mask:0xf
	v_add_f32_dpp v168, v168, v168 row_mirror row_mask:0xf bank_mask:0xf
	v_add_f32_dpp v169, v169, v169 row_mirror row_mask:0xf bank_mask:0xf
	v_add_f32_dpp v170, v170, v170 row_mirror row_mask:0xf bank_mask:0xf
	v_add_f32_dpp v171, v171, v171 row_mirror row_mask:0xf bank_mask:0xf
	v_add_f32_dpp v172, v172, v172 row_mirror row_mask:0xf bank_mask:0xf
	v_add_f32_dpp v173, v173, v173 row_mirror row_mask:0xf bank_mask:0xf
	v_add_f32_dpp v174, v174, v174 row_mirror row_mask:0xf bank_mask:0xf
	v_add_f32_dpp v175, v175, v175 row_mirror row_mask:0xf bank_mask:0xf
	v_add_f32_dpp v176, v176, v176 row_mirror row_mask:0xf bank_mask:0xf
	v_add_f32_dpp v177, v177, v177 row_mirror row_mask:0xf bank_mask:0xf
	v_mov_b32_e32 v178, v162
	v_mov_b32_e32 v179, v163
	v_mov_b32_e32 v180, v164
	v_mov_b32_e32 v181, v165
	v_mov_b32_e32 v182, v166
	v_mov_b32_e32 v183, v167
	v_mov_b32_e32 v184, v168
	v_mov_b32_e32 v185, v169
	v_mov_b32_e32 v186, v170
	v_mov_b32_e32 v187, v171
	v_mov_b32_e32 v188, v172
	v_mov_b32_e32 v189, v173
	v_mov_b32_e32 v190, v174
	v_mov_b32_e32 v191, v175
	v_mov_b32_e32 v192, v176
	v_mov_b32_e32 v193, v177
	v_permlane16_swap_b32_e32 v162, v178
	v_permlane16_swap_b32_e32 v163, v179
	v_permlane16_swap_b32_e32 v164, v180
	v_permlane16_swap_b32_e32 v165, v181
	v_permlane16_swap_b32_e32 v166, v182
	v_permlane16_swap_b32_e32 v167, v183
	v_permlane16_swap_b32_e32 v168, v184
	v_permlane16_swap_b32_e32 v169, v185
	v_permlane16_swap_b32_e32 v170, v186
	v_permlane16_swap_b32_e32 v171, v187
	v_permlane16_swap_b32_e32 v172, v188
	v_permlane16_swap_b32_e32 v173, v189
	v_permlane16_swap_b32_e32 v174, v190
	v_permlane16_swap_b32_e32 v175, v191
	v_permlane16_swap_b32_e32 v176, v192
	v_permlane16_swap_b32_e32 v177, v193
	v_add_f32_e32 v162, v162, v178
	v_add_f32_e32 v163, v163, v179
	v_add_f32_e32 v164, v164, v180
	v_add_f32_e32 v165, v165, v181
	v_add_f32_e32 v166, v166, v182
	v_add_f32_e32 v167, v167, v183
	v_add_f32_e32 v168, v168, v184
	v_add_f32_e32 v169, v169, v185
	v_add_f32_e32 v170, v170, v186
	v_add_f32_e32 v171, v171, v187
	v_add_f32_e32 v172, v172, v188
	v_add_f32_e32 v173, v173, v189
	v_add_f32_e32 v174, v174, v190
	v_add_f32_e32 v175, v175, v191
	v_add_f32_e32 v176, v176, v192
	v_add_f32_e32 v177, v177, v193
	v_fmamk_f32 v162, v162, 0x3c000000, v222
	v_fmamk_f32 v163, v163, 0x3c000000, v222
	v_fmamk_f32 v164, v164, 0x3c000000, v222
	v_fmamk_f32 v165, v165, 0x3c000000, v222
	v_fmamk_f32 v166, v166, 0x3c000000, v222
	v_fmamk_f32 v167, v167, 0x3c000000, v222
	v_fmamk_f32 v168, v168, 0x3c000000, v222
	v_fmamk_f32 v169, v169, 0x3c000000, v222
	v_fmamk_f32 v170, v170, 0x3c000000, v222
	v_fmamk_f32 v171, v171, 0x3c000000, v222
	v_fmamk_f32 v172, v172, 0x3c000000, v222
	v_fmamk_f32 v173, v173, 0x3c000000, v222
	v_fmamk_f32 v174, v174, 0x3c000000, v222
	v_fmamk_f32 v175, v175, 0x3c000000, v222
	v_fmamk_f32 v176, v176, 0x3c000000, v222
	v_fmamk_f32 v177, v177, 0x3c000000, v222
	v_rsq_f32_e32 v162, v162
	v_rsq_f32_e32 v163, v163
	v_rsq_f32_e32 v164, v164
	v_rsq_f32_e32 v165, v165
	v_rsq_f32_e32 v166, v166
	v_rsq_f32_e32 v167, v167
	v_rsq_f32_e32 v168, v168
	v_rsq_f32_e32 v169, v169
	v_rsq_f32_e32 v170, v170
	v_rsq_f32_e32 v171, v171
	v_rsq_f32_e32 v172, v172
	v_rsq_f32_e32 v173, v173
	v_rsq_f32_e32 v174, v174
	v_rsq_f32_e32 v175, v175
	v_rsq_f32_e32 v176, v176
	v_rsq_f32_e32 v177, v177
	s_waitcnt vmcnt(0)
	v_mul_f32_e32 v194, v233, v194
	v_mul_f32_e32 v195, v233, v195
	v_mul_f32_e32 v196, v233, v196
	v_mul_f32_e32 v197, v233, v197
	v_mul_f32_e32 v112, v194, v162
	v_mul_f32_e32 v113, v194, v163
	v_mul_f32_e32 v114, v194, v164
	v_mul_f32_e32 v115, v194, v165
	v_mul_f32_e32 v116, v194, v166
	v_mul_f32_e32 v117, v194, v167
	v_mul_f32_e32 v118, v194, v168
	v_mul_f32_e32 v119, v194, v169
	v_mul_f32_e32 v120, v194, v170
	v_mul_f32_e32 v121, v194, v171
	v_mul_f32_e32 v122, v194, v172
	v_mul_f32_e32 v123, v194, v173
	v_mul_f32_e32 v124, v194, v174
	v_mul_f32_e32 v125, v194, v175
	v_mul_f32_e32 v126, v194, v176
	v_mul_f32_e32 v127, v194, v177
	v_mul_f32_e32 v64, v64, v112
	v_mul_f32_e32 v65, v65, v113
	v_mul_f32_e32 v66, v66, v114
	v_mul_f32_e32 v67, v67, v115
	v_mul_f32_e32 v68, v68, v116
	v_mul_f32_e32 v69, v69, v117
	v_mul_f32_e32 v70, v70, v118
	v_mul_f32_e32 v71, v71, v119
	v_mul_f32_e32 v72, v72, v120
	v_mul_f32_e32 v73, v73, v121
	v_mul_f32_e32 v74, v74, v122
	v_mul_f32_e32 v75, v75, v123
	v_mul_f32_e32 v76, v76, v124
	v_mul_f32_e32 v77, v77, v125
	v_mul_f32_e32 v78, v78, v126
	v_mul_f32_e32 v79, v79, v127
	v_mul_f32_e32 v96, v195, v162
	v_mul_f32_e32 v97, v195, v163
	v_mul_f32_e32 v98, v195, v164
	v_mul_f32_e32 v99, v195, v165
	v_mul_f32_e32 v100, v195, v166
	v_mul_f32_e32 v101, v195, v167
	v_mul_f32_e32 v102, v195, v168
	v_mul_f32_e32 v103, v195, v169
	v_mul_f32_e32 v104, v195, v170
	v_mul_f32_e32 v105, v195, v171
	v_mul_f32_e32 v106, v195, v172
	v_mul_f32_e32 v107, v195, v173
	v_mul_f32_e32 v108, v195, v174
	v_mul_f32_e32 v109, v195, v175
	v_mul_f32_e32 v110, v195, v176
	v_mul_f32_e32 v111, v195, v177
	v_mul_f32_e32 v32, v32, v96
	v_mul_f32_e32 v33, v33, v97
	v_mul_f32_e32 v34, v34, v98
	v_mul_f32_e32 v35, v35, v99
	v_mul_f32_e32 v36, v36, v100
	v_mul_f32_e32 v37, v37, v101
	v_mul_f32_e32 v38, v38, v102
	v_mul_f32_e32 v39, v39, v103
	v_mul_f32_e32 v40, v40, v104
	v_mul_f32_e32 v41, v41, v105
	v_mul_f32_e32 v42, v42, v106
	v_mul_f32_e32 v43, v43, v107
	v_mul_f32_e32 v44, v44, v108
	v_mul_f32_e32 v45, v45, v109
	v_mul_f32_e32 v46, v46, v110
	v_mul_f32_e32 v47, v47, v111
	v_mul_f32_e32 v80, v196, v162
	v_mul_f32_e32 v81, v196, v163
	v_mul_f32_e32 v82, v196, v164
	v_mul_f32_e32 v83, v196, v165
	v_mul_f32_e32 v84, v196, v166
	v_mul_f32_e32 v85, v196, v167
	v_mul_f32_e32 v86, v196, v168
	v_mul_f32_e32 v87, v196, v169
	v_mul_f32_e32 v88, v196, v170
	v_mul_f32_e32 v89, v196, v171
	v_mul_f32_e32 v90, v196, v172
	v_mul_f32_e32 v91, v196, v173
	v_mul_f32_e32 v92, v196, v174
	v_mul_f32_e32 v93, v196, v175
	v_mul_f32_e32 v94, v196, v176
	v_mul_f32_e32 v95, v196, v177
	v_mul_f32_e32 v16, v16, v80
	v_mul_f32_e32 v17, v17, v81
	v_mul_f32_e32 v18, v18, v82
	v_mul_f32_e32 v19, v19, v83
	v_mul_f32_e32 v20, v20, v84
	v_mul_f32_e32 v21, v21, v85
	v_mul_f32_e32 v22, v22, v86
	v_mul_f32_e32 v23, v23, v87
	v_mul_f32_e32 v24, v24, v88
	v_mul_f32_e32 v25, v25, v89
	v_mul_f32_e32 v26, v26, v90
	v_mul_f32_e32 v27, v27, v91
	v_mul_f32_e32 v28, v28, v92
	v_mul_f32_e32 v29, v29, v93
	v_mul_f32_e32 v30, v30, v94
	v_mul_f32_e32 v31, v31, v95
	v_mul_f32_e32 v48, v197, v162
	v_mul_f32_e32 v49, v197, v163
	v_mul_f32_e32 v50, v197, v164
	v_mul_f32_e32 v51, v197, v165
	v_mul_f32_e32 v52, v197, v166
	v_mul_f32_e32 v53, v197, v167
	v_mul_f32_e32 v54, v197, v168
	v_mul_f32_e32 v55, v197, v169
	v_mul_f32_e32 v56, v197, v170
	v_mul_f32_e32 v57, v197, v171
	v_mul_f32_e32 v58, v197, v172
	v_mul_f32_e32 v59, v197, v173
	v_mul_f32_e32 v60, v197, v174
	v_mul_f32_e32 v61, v197, v175
	v_mul_f32_e32 v62, v197, v176
	v_mul_f32_e32 v63, v197, v177
	v_mul_f32_e32 v0, v0, v48
	v_mul_f32_e32 v1, v1, v49
	v_mul_f32_e32 v2, v2, v50
	v_mul_f32_e32 v3, v3, v51
	v_mul_f32_e32 v4, v4, v52
	v_mul_f32_e32 v5, v5, v53
	v_mul_f32_e32 v6, v6, v54
	v_mul_f32_e32 v7, v7, v55
	v_mul_f32_e32 v8, v8, v56
	v_mul_f32_e32 v9, v9, v57
	v_mul_f32_e32 v10, v10, v58
	v_mul_f32_e32 v11, v11, v59
	v_mul_f32_e32 v12, v12, v60
	v_mul_f32_e32 v13, v13, v61
	v_mul_f32_e32 v14, v14, v62
	v_mul_f32_e32 v15, v15, v63
	v_bfe_u32 v112, v64, 16, 1
	v_bfe_u32 v113, v65, 16, 1
	v_bfe_u32 v114, v66, 16, 1
	v_bfe_u32 v115, v67, 16, 1
	v_bfe_u32 v116, v68, 16, 1
	v_bfe_u32 v117, v69, 16, 1
	v_bfe_u32 v118, v70, 16, 1
	v_bfe_u32 v119, v71, 16, 1
	v_bfe_u32 v120, v72, 16, 1
	v_bfe_u32 v121, v73, 16, 1
	v_bfe_u32 v122, v74, 16, 1
	v_bfe_u32 v123, v75, 16, 1
	v_bfe_u32 v124, v76, 16, 1
	v_bfe_u32 v125, v77, 16, 1
	v_bfe_u32 v126, v78, 16, 1
	v_bfe_u32 v127, v79, 16, 1
	v_add3_u32 v64, v64, v112, s63
	v_add3_u32 v65, v65, v113, s63
	v_add3_u32 v66, v66, v114, s63
	v_add3_u32 v67, v67, v115, s63
	v_add3_u32 v68, v68, v116, s63
	v_add3_u32 v69, v69, v117, s63
	v_add3_u32 v70, v70, v118, s63
	v_add3_u32 v71, v71, v119, s63
	v_add3_u32 v72, v72, v120, s63
	v_add3_u32 v73, v73, v121, s63
	v_add3_u32 v74, v74, v122, s63
	v_add3_u32 v75, v75, v123, s63
	v_add3_u32 v76, v76, v124, s63
	v_add3_u32 v77, v77, v125, s63
	v_add3_u32 v78, v78, v126, s63
	v_add3_u32 v79, v79, v127, s63
	v_bfe_u32 v96, v32, 16, 1
	v_bfe_u32 v97, v33, 16, 1
	v_bfe_u32 v98, v34, 16, 1
	v_bfe_u32 v99, v35, 16, 1
	v_bfe_u32 v100, v36, 16, 1
	v_bfe_u32 v101, v37, 16, 1
	v_bfe_u32 v102, v38, 16, 1
	v_bfe_u32 v103, v39, 16, 1
	v_bfe_u32 v104, v40, 16, 1
	v_bfe_u32 v105, v41, 16, 1
	v_bfe_u32 v106, v42, 16, 1
	v_bfe_u32 v107, v43, 16, 1
	v_bfe_u32 v108, v44, 16, 1
	v_bfe_u32 v109, v45, 16, 1
	v_bfe_u32 v110, v46, 16, 1
	v_bfe_u32 v111, v47, 16, 1
	v_add3_u32 v32, v32, v96, s63
	v_add3_u32 v33, v33, v97, s63
	v_add3_u32 v34, v34, v98, s63
	v_add3_u32 v35, v35, v99, s63
	v_add3_u32 v36, v36, v100, s63
	v_add3_u32 v37, v37, v101, s63
	v_add3_u32 v38, v38, v102, s63
	v_add3_u32 v39, v39, v103, s63
	v_add3_u32 v40, v40, v104, s63
	v_add3_u32 v41, v41, v105, s63
	v_add3_u32 v42, v42, v106, s63
	v_add3_u32 v43, v43, v107, s63
	v_add3_u32 v44, v44, v108, s63
	v_add3_u32 v45, v45, v109, s63
	v_add3_u32 v46, v46, v110, s63
	v_add3_u32 v47, v47, v111, s63
	v_bfe_u32 v80, v16, 16, 1
	v_bfe_u32 v81, v17, 16, 1
	v_bfe_u32 v82, v18, 16, 1
	v_bfe_u32 v83, v19, 16, 1
	v_bfe_u32 v84, v20, 16, 1
	v_bfe_u32 v85, v21, 16, 1
	v_bfe_u32 v86, v22, 16, 1
	v_bfe_u32 v87, v23, 16, 1
	v_bfe_u32 v88, v24, 16, 1
	v_bfe_u32 v89, v25, 16, 1
	v_bfe_u32 v90, v26, 16, 1
	v_bfe_u32 v91, v27, 16, 1
	v_bfe_u32 v92, v28, 16, 1
	v_bfe_u32 v93, v29, 16, 1
	v_bfe_u32 v94, v30, 16, 1
	v_bfe_u32 v95, v31, 16, 1
	v_add3_u32 v16, v16, v80, s63
	v_add3_u32 v17, v17, v81, s63
	v_add3_u32 v18, v18, v82, s63
	v_add3_u32 v19, v19, v83, s63
	v_add3_u32 v20, v20, v84, s63
	v_add3_u32 v21, v21, v85, s63
	v_add3_u32 v22, v22, v86, s63
	v_add3_u32 v23, v23, v87, s63
	v_add3_u32 v24, v24, v88, s63
	v_add3_u32 v25, v25, v89, s63
	v_add3_u32 v26, v26, v90, s63
	v_add3_u32 v27, v27, v91, s63
	v_add3_u32 v28, v28, v92, s63
	v_add3_u32 v29, v29, v93, s63
	v_add3_u32 v30, v30, v94, s63
	v_add3_u32 v31, v31, v95, s63
	v_bfe_u32 v48, v0, 16, 1
	v_bfe_u32 v49, v1, 16, 1
	v_bfe_u32 v50, v2, 16, 1
	v_bfe_u32 v51, v3, 16, 1
	v_bfe_u32 v52, v4, 16, 1
	v_bfe_u32 v53, v5, 16, 1
	v_bfe_u32 v54, v6, 16, 1
	v_bfe_u32 v55, v7, 16, 1
	v_bfe_u32 v56, v8, 16, 1
	v_bfe_u32 v57, v9, 16, 1
	v_bfe_u32 v58, v10, 16, 1
	v_bfe_u32 v59, v11, 16, 1
	v_bfe_u32 v60, v12, 16, 1
	v_bfe_u32 v61, v13, 16, 1
	v_bfe_u32 v62, v14, 16, 1
	v_bfe_u32 v63, v15, 16, 1
	v_add3_u32 v0, v0, v48, s63
	v_add3_u32 v1, v1, v49, s63
	v_add3_u32 v2, v2, v50, s63
	v_add3_u32 v3, v3, v51, s63
	v_add3_u32 v4, v4, v52, s63
	v_add3_u32 v5, v5, v53, s63
	v_add3_u32 v6, v6, v54, s63
	v_add3_u32 v7, v7, v55, s63
	v_add3_u32 v8, v8, v56, s63
	v_add3_u32 v9, v9, v57, s63
	v_add3_u32 v10, v10, v58, s63
	v_add3_u32 v11, v11, v59, s63
	v_add3_u32 v12, v12, v60, s63
	v_add3_u32 v13, v13, v61, s63
	v_add3_u32 v14, v14, v62, s63
	v_add3_u32 v15, v15, v63, s63
	s_lshl_b32 s16, s38, 8
	s_add_i32 s16, s16, s65
	v_lshlrev_b32_e32 v200, 10, v128
	v_lshl_add_u32 v200, v199, 1, v200
	v_add_u32_e32 v200, s16, v200
	ds_write_b16_d16_hi v200, v64 offset:0
	ds_write_b16_d16_hi v200, v32 offset:64
	ds_write_b16_d16_hi v200, v16 offset:128
	ds_write_b16_d16_hi v200, v0 offset:192
	ds_write_b16_d16_hi v200, v65 offset:256
	ds_write_b16_d16_hi v200, v33 offset:320
	ds_write_b16_d16_hi v200, v17 offset:384
	ds_write_b16_d16_hi v200, v1 offset:448
	ds_write_b16_d16_hi v200, v66 offset:512
	ds_write_b16_d16_hi v200, v34 offset:576
	ds_write_b16_d16_hi v200, v18 offset:640
	ds_write_b16_d16_hi v200, v2 offset:704
	ds_write_b16_d16_hi v200, v67 offset:768
	ds_write_b16_d16_hi v200, v35 offset:832
	ds_write_b16_d16_hi v200, v19 offset:896
	ds_write_b16_d16_hi v200, v3 offset:960
	ds_write_b16_d16_hi v200, v68 offset:2048
	ds_write_b16_d16_hi v200, v36 offset:2112
	ds_write_b16_d16_hi v200, v20 offset:2176
	ds_write_b16_d16_hi v200, v4 offset:2240
	ds_write_b16_d16_hi v200, v69 offset:2304
	ds_write_b16_d16_hi v200, v37 offset:2368
	ds_write_b16_d16_hi v200, v21 offset:2432
	ds_write_b16_d16_hi v200, v5 offset:2496
	ds_write_b16_d16_hi v200, v70 offset:2560
	ds_write_b16_d16_hi v200, v38 offset:2624
	ds_write_b16_d16_hi v200, v22 offset:2688
	ds_write_b16_d16_hi v200, v6 offset:2752
	ds_write_b16_d16_hi v200, v71 offset:2816
	ds_write_b16_d16_hi v200, v39 offset:2880
	ds_write_b16_d16_hi v200, v23 offset:2944
	ds_write_b16_d16_hi v200, v7 offset:3008
	ds_write_b16_d16_hi v200, v72 offset:4096
	ds_write_b16_d16_hi v200, v40 offset:4160
	ds_write_b16_d16_hi v200, v24 offset:4224
	ds_write_b16_d16_hi v200, v8 offset:4288
	ds_write_b16_d16_hi v200, v73 offset:4352
	ds_write_b16_d16_hi v200, v41 offset:4416
	ds_write_b16_d16_hi v200, v25 offset:4480
	ds_write_b16_d16_hi v200, v9 offset:4544
	ds_write_b16_d16_hi v200, v74 offset:4608
	ds_write_b16_d16_hi v200, v42 offset:4672
	ds_write_b16_d16_hi v200, v26 offset:4736
	ds_write_b16_d16_hi v200, v10 offset:4800
	ds_write_b16_d16_hi v200, v75 offset:4864
	ds_write_b16_d16_hi v200, v43 offset:4928
	ds_write_b16_d16_hi v200, v27 offset:4992
	ds_write_b16_d16_hi v200, v11 offset:5056
	ds_write_b16_d16_hi v200, v76 offset:6144
	ds_write_b16_d16_hi v200, v44 offset:6208
	ds_write_b16_d16_hi v200, v28 offset:6272
	ds_write_b16_d16_hi v200, v12 offset:6336
	ds_write_b16_d16_hi v200, v77 offset:6400
	ds_write_b16_d16_hi v200, v45 offset:6464
	ds_write_b16_d16_hi v200, v29 offset:6528
	ds_write_b16_d16_hi v200, v13 offset:6592
	ds_write_b16_d16_hi v200, v78 offset:6656
	ds_write_b16_d16_hi v200, v46 offset:6720
	ds_write_b16_d16_hi v200, v30 offset:6784
	ds_write_b16_d16_hi v200, v14 offset:6848
	ds_write_b16_d16_hi v200, v79 offset:6912
	ds_write_b16_d16_hi v200, v47 offset:6976
	ds_write_b16_d16_hi v200, v31 offset:7040
	ds_write_b16_d16_hi v200, v15 offset:7104
	v_lshrrev_b32_e32 v201, 4, v235
	v_and_b32_e32 v204, 15, v235
	v_lshlrev_b32_e32 v208, 4, v204
	v_lshl_add_u32 v205, v201, 8, v208
	v_add_u32_e32 v205, s16, v205
	v_add_u32_e32 v206, s38, v201
	v_lshl_add_u64 v[202:203], s[14:15], 0, v[208:209]
	v_mad_i64_i32 v[202:203], s[16:17], v206, s62, v[202:203]
	s_lshl_b32 s16, s62, 2
	s_mov_b32 s17, 0
	ds_read_b128 v[96:99], v205 offset:0
	ds_read_b128 v[100:103], v205 offset:1024
	ds_read_b128 v[104:107], v205 offset:2048
	ds_read_b128 v[108:111], v205 offset:3072
	ds_read_b128 v[112:115], v205 offset:4096
	ds_read_b128 v[116:119], v205 offset:5120
	ds_read_b128 v[120:123], v205 offset:6144
	ds_read_b128 v[124:127], v205 offset:7168
	s_waitcnt lgkmcnt(7)
	global_store_dwordx4 v[202:203], v[96:99], off
	v_lshl_add_u64 v[202:203], v[202:203], 0, s[16:17]
	s_waitcnt lgkmcnt(6)
	global_store_dwordx4 v[202:203], v[100:103], off
	v_lshl_add_u64 v[202:203], v[202:203], 0, s[16:17]
	s_waitcnt lgkmcnt(5)
	global_store_dwordx4 v[202:203], v[104:107], off
	v_lshl_add_u64 v[202:203], v[202:203], 0, s[16:17]
	s_waitcnt lgkmcnt(4)
	global_store_dwordx4 v[202:203], v[108:111], off
	v_lshl_add_u64 v[202:203], v[202:203], 0, s[16:17]
	s_waitcnt lgkmcnt(3)
	global_store_dwordx4 v[202:203], v[112:115], off
	v_lshl_add_u64 v[202:203], v[202:203], 0, s[16:17]
	s_waitcnt lgkmcnt(2)
	global_store_dwordx4 v[202:203], v[116:119], off
	v_lshl_add_u64 v[202:203], v[202:203], 0, s[16:17]
	s_waitcnt lgkmcnt(1)
	global_store_dwordx4 v[202:203], v[120:123], off
	v_lshl_add_u64 v[202:203], v[202:203], 0, s[16:17]
	s_waitcnt lgkmcnt(0)
	global_store_dwordx4 v[202:203], v[124:127], off
	s_mov_b64 s[14:15], 0
	s_and_b64 vcc, exec, s[12:13]
	s_waitcnt vmcnt(63) expcnt(7) lgkmcnt(15)
	s_barrier
	s_cbranch_vccnz .LBB0_559
